# nt hint also on the RWKV chain's ring (LDS-DMA) loads of the read-once chunk records
# baseline (speedup 1.0000x reference)
.LBB0_820:
	s_add_u32 s50, s61, 0x796f3000
	s_addc_u32 s51, s62, 0
	s_add_i32 m0, s60, 0xffffa800
	s_nop 0
	global_load_lds_dwordx4 v[24:25], off nt
	v_mov_b32_e32 v24, s50
	v_cndmask_b32_e64 v24, v24, v22, s[40:41]
	v_mov_b32_e32 v22, s51
	v_cndmask_b32_e64 v23, v22, v23, s[40:41]
	v_mov_b32_e32 v25, s49
	v_cndmask_b32_e64 v25, v23, v25, s[0:1]
	v_mov_b32_e32 v23, s48
	v_cndmask_b32_e64 v22, v9, v29, s[0:1]
	v_cndmask_b32_e64 v24, v24, v23, s[0:1]
	s_and_b64 s[0:1], s[0:1], exec
	v_ashrrev_i32_e32 v23, 31, v22
	s_cselect_b32 s0, 4, s34
	v_lshlrev_b64 v[22:23], s0, v[22:23]
	v_lshl_add_u64 v[22:23], v[24:25], 0, v[22:23]
	s_add_i32 m0, s60, 0xffffac00
	s_andn2_b64 vcc, exec, s[18:19]
	global_load_lds_dwordx4 v[22:23], off nt
	s_cbranch_vccz .LBB0_829

.LBB0_822:
	s_mul_i32 s0, s35, 0x5c00
	s_add_u32 s50, s52, s0
	s_addc_u32 s51, s53, 0
	s_add_u32 s61, s36, s46
	s_addc_u32 s62, s37, s47
	s_add_u32 s0, s61, 0x796f0400
	s_addc_u32 s1, s62, 0
	v_lshl_add_u64 v[22:23], v[18:19], 0, s[46:47]
	s_mov_b64 s[6:7], 0x796f4000
	s_add_u32 s48, s61, 0x796f2400
	v_lshl_add_u64 v[22:23], v[22:23], 0, s[6:7]
	s_addc_u32 s49, s62, 0
	v_mov_b32_e32 v24, s48
	v_cndmask_b32_e64 v29, v24, v22, s[4:5]
	v_mov_b32_e32 v24, s49
	v_cndmask_b32_e64 v30, v24, v23, s[4:5]
	v_mov_b32_e32 v31, s1
	v_mov_b32_e32 v32, s0
	v_cndmask_b32_e64 v25, v30, v31, s[42:43]
	v_cndmask_b32_e64 v24, v29, v32, s[42:43]
	s_add_i32 s60, s59, s45
	v_lshl_add_u64 v[24:25], v[24:25], 0, v[12:13]
	s_add_i32 m0, s60, 0xffffa000
	s_andn2_b64 vcc, exec, s[14:15]
	global_load_lds_dwordx4 v[24:25], off nt
	v_cndmask_b32_e64 v25, v30, v31, s[2:3]
	v_cndmask_b32_e64 v24, v29, v32, s[2:3]
	v_lshl_add_u64 v[24:25], v[24:25], 0, v[14:15]
	s_add_i32 m0, s60, 0xffffa400
	s_mov_b64 s[0:1], -1
	global_load_lds_dwordx4 v[24:25], off nt
	s_cbranch_vccnz .LBB0_835
	s_andn2_b64 vcc, exec, s[24:25]
	s_cbranch_vccnz .LBB0_832
	s_andn2_b64 vcc, exec, s[26:27]
	s_cbranch_vccnz .LBB0_830
	s_andn2_b64 vcc, exec, s[28:29]
	s_cbranch_vccnz .LBB0_827
	v_lshl_add_u64 v[24:25], s[50:51], 0, v[40:41]
	s_mov_b64 s[0:1], 0x2c00
	v_lshl_add_u64 v[24:25], v[24:25], 0, s[0:1]
	s_mov_b64 s[0:1], 0

.LBB0_829:
	v_lshl_add_u64 v[22:23], v[20:21], 0, s[46:47]
	s_mov_b32 m0, s59
	s_nop 0
	global_load_lds_dwordx4 v[22:23], off nt
	s_branch .LBB0_821

.LBB0_839:
	s_add_u32 s46, s59, 0x7970fc00
	s_addc_u32 s47, s60, 0
	s_add_i32 m0, s58, s51
	s_nop 0
	global_load_lds_dwordx4 v[20:21], off nt
	v_mov_b32_e32 v20, s46
	v_cndmask_b32_e64 v20, v20, v18, s[40:41]
	v_mov_b32_e32 v18, s47
	v_cndmask_b32_e64 v19, v18, v19, s[40:41]
	v_mov_b32_e32 v21, s49
	v_cndmask_b32_e64 v21, v19, v21, s[0:1]
	v_mov_b32_e32 v19, s48
	v_cndmask_b32_e64 v18, v62, v22, s[0:1]
	v_cndmask_b32_e64 v20, v20, v19, s[0:1]
	s_and_b64 s[0:1], s[0:1], exec
	v_ashrrev_i32_e32 v19, 31, v18
	s_cselect_b32 s0, 4, s34
	v_lshlrev_b64 v[18:19], s0, v[18:19]
	v_lshl_add_u64 v[18:19], v[20:21], 0, v[18:19]
	s_add_i32 m0, s58, s54
	s_andn2_b64 vcc, exec, s[18:19]
	global_load_lds_dwordx4 v[18:19], off nt
	s_cbranch_vccz .LBB0_867

.LBB0_858:
	s_cmpk_gt_u32 s46, 0x10a
	s_cbranch_scc1 .LBB0_840
	s_mul_i32 s0, s57, 0x5c00
	s_add_i32 s0, s0, 0x1cc00
	s_add_u32 s46, s52, s0
	s_addc_u32 s47, s53, 0
	s_add_u32 s59, s42, s44
	s_addc_u32 s60, s43, s45
	s_add_u32 s61, s59, 0x7970d000
	s_mul_i32 s0, s55, 0x2493
	s_addc_u32 s62, s60, 0
	s_lshr_b32 s0, s0, 16
	s_sub_i32 s1, s55, s0
	s_bfe_u32 s1, s1, 0xf0001
	s_add_i32 s1, s1, s0
	s_bfe_u32 s0, s1, 0xe0002
	s_mul_i32 s0, s0, 7
	s_sub_i32 s0, s55, s0
	s_and_b32 s0, s0, 0xffff
	s_mulk_i32 s0, 0x4400
	s_add_i32 s58, s0, 0
	s_add_u32 s48, s59, 0x7970f000
	v_lshl_add_u64 v[18:19], v[54:55], 0, s[44:45]
	s_mov_b64 s[0:1], 0x79710c00
	s_addc_u32 s49, s60, 0
	v_lshl_add_u64 v[18:19], v[18:19], 0, s[0:1]
	s_and_b64 s[0:1], s[2:3], exec
	s_cselect_b32 s1, s62, s49
	s_cselect_b32 s0, s61, s48
	v_mov_b32_e32 v20, s1
	v_cndmask_b32_e64 v21, v20, v19, s[4:5]
	v_mov_b32_e32 v20, s0
	v_cndmask_b32_e64 v20, v20, v18, s[4:5]
	v_lshl_add_u64 v[20:21], v[20:21], 0, v[48:49]
	s_add_i32 m0, s58, s35
	v_mov_b32_e32 v22, s62
	global_load_lds_dwordx4 v[20:21], off nt
	v_mov_b32_e32 v21, s49
	v_mov_b32_e32 v20, s48
	v_cndmask_b32_e64 v21, v19, v21, s[38:39]
	v_cndmask_b32_e64 v20, v18, v20, s[38:39]
	v_cndmask_b32_e64 v21, v21, v22, s[2:3]
	v_mov_b32_e32 v22, s61
	v_cndmask_b32_e64 v20, v20, v22, s[2:3]
	v_lshl_add_u64 v[20:21], v[20:21], 0, v[50:51]
	s_add_i32 m0, s58, s50
	s_andn2_b64 vcc, exec, s[14:15]
	global_load_lds_dwordx4 v[20:21], off nt
	s_mov_b64 s[0:1], -1
	s_cbranch_vccnz .LBB0_873
	s_andn2_b64 vcc, exec, s[24:25]
	s_cbranch_vccnz .LBB0_870
	s_andn2_b64 vcc, exec, s[26:27]
	s_cbranch_vccnz .LBB0_868
	s_andn2_b64 vcc, exec, s[28:29]
	s_cbranch_vccnz .LBB0_864
	v_lshl_add_u64 v[20:21], s[46:47], 0, v[40:41]
	s_mov_b64 s[0:1], 0x2c00
	v_lshl_add_u64 v[20:21], v[20:21], 0, s[0:1]
	s_mov_b64 s[0:1], 0

.LBB0_867:
	s_add_i32 m0, s58, 0x4000
	v_lshl_add_u64 v[18:19], v[56:57], 0, s[44:45]
	global_load_lds_dwordx4 v[18:19], off nt
	s_branch .LBB0_840
